# x14v2: phase-14 row pass on idle workgroups during the scan (ascending readiness order, prefetch, seam 14 dropped)
# baseline (speedup 1.0000x reference)
.Lx14_sb_done:
	s_or_b64 exec, exec, s[98:99]
	s_barrier
	v_mbcnt_lo_u32_b32 v1, -1, 0
	v_mbcnt_hi_u32_b32 v1, -1, v1
	v_lshlrev_b32_e32 v2, 4, v1
	v_lshrrev_b32_e32 v3, 3, v1
	v_lshlrev_b32_e32 v3, 2, v3
	v_and_b32_e32 v4, 31, v1
	v_lshlrev_b32_e32 v4, 2, v4
	v_lshrrev_b32_e32 v9, 5, v1
	v_lshl_add_u32 v4, v9, 8, v4
	v_lshlrev_b32_e32 v9, 5, v1
	s_load_dwordx4 s[28:31], s[74:75], 0x100
	s_add_u32 s4, s54, 0x8c00000
	s_addc_u32 s5, s55, 0
	s_add_u32 s6, s54, 0x29400000
	s_addc_u32 s7, s55, 0
	s_add_u32 s8, s54, 0x21200000
	s_addc_u32 s9, s55, 0
	s_add_u32 s10, s54, 0x49c00000
	s_addc_u32 s11, s55, 0
	s_add_u32 s12, s54, 0x19000000
	s_addc_u32 s13, s55, 0
	s_add_u32 s14, s54, 0xc00000
	s_addc_u32 s15, s55, 0
	s_add_u32 s16, s54, 0x1000000
	s_addc_u32 s17, s55, 0
	s_add_u32 s20, s54, 0xc400
	s_addc_u32 s21, s55, 0
	s_mov_b32 s18, -1
	s_mov_b32 s19, 0
	s_add_i32 s25, s2, 0xffffff80
	s_lshl_b32 s25, s25, 3
	s_add_i32 s25, s25, s82
	s_lshr_b32 s100, s25, 8
	s_and_b32 s25, s25, 0xff
	s_mov_b32 s24, 0
	s_mov_b32 s26, 0
	s_waitcnt lgkmcnt(0)
	global_load_dwordx4 v[10:13], v9, s[28:29]
	global_load_dwordx4 v[14:17], v9, s[28:29] offset:16
	global_load_dwordx4 v[18:21], v9, s[28:29] offset:2048
	global_load_dwordx4 v[22:25], v9, s[28:29] offset:2064
	global_load_dwordx4 v[42:45], v9, s[30:31]
	global_load_dwordx4 v[46:49], v9, s[30:31] offset:16
	global_load_dwordx4 v[50:53], v9, s[30:31] offset:2048
	global_load_dwordx4 v[54:57], v9, s[30:31] offset:2064
	v_add_u32_e32 v9, 0x1000, v9
	global_load_dwordx4 v[26:29], v9, s[28:29]
	global_load_dwordx4 v[30:33], v9, s[28:29] offset:16
	global_load_dwordx4 v[34:37], v9, s[28:29] offset:2048
	global_load_dwordx4 v[38:41], v9, s[28:29] offset:2064
	global_load_dwordx4 v[58:61], v9, s[30:31]
	global_load_dwordx4 v[62:65], v9, s[30:31] offset:16
	global_load_dwordx4 v[66:69], v9, s[30:31] offset:2048
	global_load_dwordx4 v[70:73], v9, s[30:31] offset:2064
	s_waitcnt vmcnt(0)
.Lx14_row:
	s_lshr_b32 s0, s24, 2
	s_and_b32 s1, s24, 3
	s_lshl_b32 s0, s0, 10
	s_lshl_b32 s3, s1, 8
	s_add_i32 s0, s0, s3
	s_add_i32 s0, s0, s25
	s_sub_i32 s1, s1, s100
	s_and_b32 s1, s1, 3
	s_lshr_b32 s3, s1, 1
	s_and_b32 s1, s1, 1
	s_sub_i32 s28, 0x1fff, s0
	s_add_i32 s29, s0, 0x2000
	s_cmp_lg_u32 s1, 0
	s_cselect_b32 s28, s29, s28
	s_add_i32 s29, s28, 0x100
	s_lshr_b32 s29, s29, 6
	s_add_i32 s29, s29, 1
	s_sub_i32 s30, 0x40ff, s28
	s_lshr_b32 s30, s30, 6
	s_add_i32 s30, s30, 1
	s_lshl_b32 s31, s3, 14
	s_add_i32 s31, s31, s28
	s_lshl_b32 s3, s3, 7
	v_add_u32_e32 v7, s3, v4
	v_mov_b32_e32 v8, s30
	v_mov_b32_e32 v9, s29
	v_cndmask_b32_e64 v8, v8, v9, s[18:19]
	s_lshl_b32 s0, s31, 12
	v_add_u32_e32 v5, s0, v2
	s_lshl_b32 s1, s31, 7
	v_add_u32_e32 v6, s1, v3
	global_load_dwordx4 v[112:115], v5, s[8:9]
	global_load_dwordx4 v[116:119], v5, s[8:9] offset:1024
	global_load_dwordx4 v[120:123], v5, s[8:9] offset:2048
	global_load_dwordx4 v[124:127], v5, s[8:9] offset:3072
	global_load_dwordx4 v[128:131], v5, s[10:11]
	global_load_dwordx4 v[132:135], v5, s[10:11] offset:1024
	global_load_dwordx4 v[136:139], v5, s[10:11] offset:2048
	global_load_dwordx4 v[140:143], v5, s[10:11] offset:3072
	global_load_dword v144, v6, s[14:15]
	global_load_dword v145, v6, s[14:15] offset:32
	global_load_dword v146, v6, s[14:15] offset:64
	global_load_dword v147, v6, s[14:15] offset:96
	global_load_dword v148, v6, s[16:17]
	global_load_dword v149, v6, s[16:17] offset:32
	global_load_dword v150, v6, s[16:17] offset:64
	global_load_dword v151, v6, s[16:17] offset:96
	s_cmp_lg_u32 s26, 0
	s_cbranch_scc1 .Lx14_ready
	s_mov_b32 s27, 0

.Lx14_ready:
	global_load_dwordx4 v[80:83], v5, s[4:5] sc1
	global_load_dwordx4 v[84:87], v5, s[4:5] offset:1024 sc1
	global_load_dwordx4 v[88:91], v5, s[4:5] offset:2048 sc1
	global_load_dwordx4 v[92:95], v5, s[4:5] offset:3072 sc1
	global_load_dwordx4 v[96:99], v5, s[6:7] sc1
	global_load_dwordx4 v[100:103], v5, s[6:7] offset:1024 sc1
	global_load_dwordx4 v[104:107], v5, s[6:7] offset:2048 sc1
	global_load_dwordx4 v[108:111], v5, s[6:7] offset:3072 sc1
	s_waitcnt vmcnt(0)
	v_lshlrev_b32_e32 v168, 16, v80
	v_lshlrev_b32_e32 v169, 16, v96
	v_add_f32_e32 v160, v168, v169
	v_and_b32_e32 v168, 0xffff0000, v80
	v_and_b32_e32 v169, 0xffff0000, v96
	v_add_f32_e32 v161, v168, v169
	v_lshlrev_b32_e32 v168, 16, v81
	v_lshlrev_b32_e32 v169, 16, v97
	v_add_f32_e32 v162, v168, v169
	v_and_b32_e32 v168, 0xffff0000, v81
	v_and_b32_e32 v169, 0xffff0000, v97
	v_add_f32_e32 v163, v168, v169
	v_lshlrev_b32_e32 v168, 16, v82
	v_lshlrev_b32_e32 v169, 16, v98
	v_add_f32_e32 v164, v168, v169
	v_and_b32_e32 v168, 0xffff0000, v82
	v_and_b32_e32 v169, 0xffff0000, v98
	v_add_f32_e32 v165, v168, v169
	v_lshlrev_b32_e32 v168, 16, v83
	v_lshlrev_b32_e32 v169, 16, v99
	v_add_f32_e32 v166, v168, v169
	v_and_b32_e32 v168, 0xffff0000, v83
	v_and_b32_e32 v169, 0xffff0000, v99
	v_add_f32_e32 v167, v168, v169
	v_add_f32_e32 v170, v160, v161
	v_add_f32_e32 v170, v170, v162
	v_add_f32_e32 v170, v170, v163
	v_add_f32_e32 v170, v170, v164
	v_add_f32_e32 v170, v170, v165
	v_add_f32_e32 v170, v170, v166
	v_add_f32_e32 v170, v170, v167
	s_nop 1
	v_add_f32_dpp v170, v170, v170 quad_perm:[1,0,3,2] row_mask:0xf bank_mask:0xf bound_ctrl:1
	s_nop 1
	v_add_f32_dpp v170, v170, v170 quad_perm:[2,3,0,1] row_mask:0xf bank_mask:0xf bound_ctrl:1
	s_nop 1
	v_add_f32_dpp v170, v170, v170 row_half_mirror row_mask:0xf bank_mask:0xf bound_ctrl:1
	v_mul_f32_e32 v170, 0x3c800000, v170
	v_sub_f32_e32 v160, v160, v170
	v_sub_f32_e32 v161, v161, v170
	v_sub_f32_e32 v162, v162, v170
	v_sub_f32_e32 v163, v163, v170
	v_sub_f32_e32 v164, v164, v170
	v_sub_f32_e32 v165, v165, v170
	v_sub_f32_e32 v166, v166, v170
	v_sub_f32_e32 v167, v167, v170
	v_mul_f32_e32 v171, v160, v160
	v_fmac_f32_e32 v171, v161, v161
	v_fmac_f32_e32 v171, v162, v162
	v_fmac_f32_e32 v171, v163, v163
	v_fmac_f32_e32 v171, v164, v164
	v_fmac_f32_e32 v171, v165, v165
	v_fmac_f32_e32 v171, v166, v166
	v_fmac_f32_e32 v171, v167, v167
	s_nop 1
	v_add_f32_dpp v171, v171, v171 quad_perm:[1,0,3,2] row_mask:0xf bank_mask:0xf bound_ctrl:1
	s_nop 1
	v_add_f32_dpp v171, v171, v171 quad_perm:[2,3,0,1] row_mask:0xf bank_mask:0xf bound_ctrl:1
	s_nop 1
	v_add_f32_dpp v171, v171, v171 row_half_mirror row_mask:0xf bank_mask:0xf bound_ctrl:1
	v_mov_b32_e32 v172, 0x3a27c5ac
	v_fmac_f32_e32 v172, 0x3c800000, v171
	v_rsq_f32_e32 v172, v172
	v_add_f32_e32 v173, v144, v148
	s_nop 0
	v_mul_f32_e32 v160, v160, v172
	v_mul_f32_e32 v161, v161, v172
	v_mul_f32_e32 v162, v162, v172
	v_mul_f32_e32 v163, v163, v172
	v_mul_f32_e32 v164, v164, v172
	v_mul_f32_e32 v165, v165, v172
	v_mul_f32_e32 v166, v166, v172
	v_mul_f32_e32 v167, v167, v172
	v_fma_f32 v160, v10, v160, v42
	v_fma_f32 v161, v11, v161, v43
	v_fma_f32 v162, v12, v162, v44
	v_fma_f32 v163, v13, v163, v45
	v_fma_f32 v164, v14, v164, v46
	v_fma_f32 v165, v15, v165, v47
	v_fma_f32 v166, v16, v166, v48
	v_fma_f32 v167, v17, v167, v49
	v_lshlrev_b32_e32 v168, 16, v112
	v_fmac_f32_e32 v160, v173, v168
	v_and_b32_e32 v169, 0xffff0000, v112
	v_fmac_f32_e32 v161, v173, v169
	v_lshlrev_b32_e32 v168, 16, v128
	v_mul_f32_e32 v160, v160, v168
	v_and_b32_e32 v169, 0xffff0000, v128
	v_mul_f32_e32 v161, v161, v169
	v_lshlrev_b32_e32 v168, 16, v113
	v_fmac_f32_e32 v162, v173, v168
	v_and_b32_e32 v169, 0xffff0000, v113
	v_fmac_f32_e32 v163, v173, v169
	v_lshlrev_b32_e32 v168, 16, v129
	v_mul_f32_e32 v162, v162, v168
	v_and_b32_e32 v169, 0xffff0000, v129
	v_mul_f32_e32 v163, v163, v169
	v_lshlrev_b32_e32 v168, 16, v114
	v_fmac_f32_e32 v164, v173, v168
	v_and_b32_e32 v169, 0xffff0000, v114
	v_fmac_f32_e32 v165, v173, v169
	v_lshlrev_b32_e32 v168, 16, v130
	v_mul_f32_e32 v164, v164, v168
	v_and_b32_e32 v169, 0xffff0000, v130
	v_mul_f32_e32 v165, v165, v169
	v_lshlrev_b32_e32 v168, 16, v115
	v_fmac_f32_e32 v166, v173, v168
	v_and_b32_e32 v169, 0xffff0000, v115
	v_fmac_f32_e32 v167, v173, v169
	v_lshlrev_b32_e32 v168, 16, v131
	v_mul_f32_e32 v166, v166, v168
	v_and_b32_e32 v169, 0xffff0000, v131
	v_mul_f32_e32 v167, v167, v169
	v_cvt_pk_bf16_f32 v180, v160, v161
	v_cvt_pk_bf16_f32 v181, v162, v163
	v_cvt_pk_bf16_f32 v182, v164, v165
	v_cvt_pk_bf16_f32 v183, v166, v167
	global_store_dwordx4 v5, v[180:183], s[12:13]
	v_lshlrev_b32_e32 v168, 16, v84
	v_lshlrev_b32_e32 v169, 16, v100
	v_add_f32_e32 v160, v168, v169
	v_and_b32_e32 v168, 0xffff0000, v84
	v_and_b32_e32 v169, 0xffff0000, v100
	v_add_f32_e32 v161, v168, v169
	v_lshlrev_b32_e32 v168, 16, v85
	v_lshlrev_b32_e32 v169, 16, v101
	v_add_f32_e32 v162, v168, v169
	v_and_b32_e32 v168, 0xffff0000, v85
	v_and_b32_e32 v169, 0xffff0000, v101
	v_add_f32_e32 v163, v168, v169
	v_lshlrev_b32_e32 v168, 16, v86
	v_lshlrev_b32_e32 v169, 16, v102
	v_add_f32_e32 v164, v168, v169
	v_and_b32_e32 v168, 0xffff0000, v86
	v_and_b32_e32 v169, 0xffff0000, v102
	v_add_f32_e32 v165, v168, v169
	v_lshlrev_b32_e32 v168, 16, v87
	v_lshlrev_b32_e32 v169, 16, v103
	v_add_f32_e32 v166, v168, v169
	v_and_b32_e32 v168, 0xffff0000, v87
	v_and_b32_e32 v169, 0xffff0000, v103
	v_add_f32_e32 v167, v168, v169
	v_add_f32_e32 v170, v160, v161
	v_add_f32_e32 v170, v170, v162
	v_add_f32_e32 v170, v170, v163
	v_add_f32_e32 v170, v170, v164
	v_add_f32_e32 v170, v170, v165
	v_add_f32_e32 v170, v170, v166
	v_add_f32_e32 v170, v170, v167
	s_nop 1
	v_add_f32_dpp v170, v170, v170 quad_perm:[1,0,3,2] row_mask:0xf bank_mask:0xf bound_ctrl:1
	s_nop 1
	v_add_f32_dpp v170, v170, v170 quad_perm:[2,3,0,1] row_mask:0xf bank_mask:0xf bound_ctrl:1
	s_nop 1
	v_add_f32_dpp v170, v170, v170 row_half_mirror row_mask:0xf bank_mask:0xf bound_ctrl:1
	v_mul_f32_e32 v170, 0x3c800000, v170
	v_sub_f32_e32 v160, v160, v170
	v_sub_f32_e32 v161, v161, v170
	v_sub_f32_e32 v162, v162, v170
	v_sub_f32_e32 v163, v163, v170
	v_sub_f32_e32 v164, v164, v170
	v_sub_f32_e32 v165, v165, v170
	v_sub_f32_e32 v166, v166, v170
	v_sub_f32_e32 v167, v167, v170
	v_mul_f32_e32 v171, v160, v160
	v_fmac_f32_e32 v171, v161, v161
	v_fmac_f32_e32 v171, v162, v162
	v_fmac_f32_e32 v171, v163, v163
	v_fmac_f32_e32 v171, v164, v164
	v_fmac_f32_e32 v171, v165, v165
	v_fmac_f32_e32 v171, v166, v166
	v_fmac_f32_e32 v171, v167, v167
	s_nop 1
	v_add_f32_dpp v171, v171, v171 quad_perm:[1,0,3,2] row_mask:0xf bank_mask:0xf bound_ctrl:1
	s_nop 1
	v_add_f32_dpp v171, v171, v171 quad_perm:[2,3,0,1] row_mask:0xf bank_mask:0xf bound_ctrl:1
	s_nop 1
	v_add_f32_dpp v171, v171, v171 row_half_mirror row_mask:0xf bank_mask:0xf bound_ctrl:1
	v_mov_b32_e32 v172, 0x3a27c5ac
	v_fmac_f32_e32 v172, 0x3c800000, v171
	v_rsq_f32_e32 v172, v172
	v_add_f32_e32 v173, v145, v149
	s_nop 0
	v_mul_f32_e32 v160, v160, v172
	v_mul_f32_e32 v161, v161, v172
	v_mul_f32_e32 v162, v162, v172
	v_mul_f32_e32 v163, v163, v172
	v_mul_f32_e32 v164, v164, v172
	v_mul_f32_e32 v165, v165, v172
	v_mul_f32_e32 v166, v166, v172
	v_mul_f32_e32 v167, v167, v172
	v_fma_f32 v160, v18, v160, v50
	v_fma_f32 v161, v19, v161, v51
	v_fma_f32 v162, v20, v162, v52
	v_fma_f32 v163, v21, v163, v53
	v_fma_f32 v164, v22, v164, v54
	v_fma_f32 v165, v23, v165, v55
	v_fma_f32 v166, v24, v166, v56
	v_fma_f32 v167, v25, v167, v57
	v_lshlrev_b32_e32 v168, 16, v116
	v_fmac_f32_e32 v160, v173, v168
	v_and_b32_e32 v169, 0xffff0000, v116
	v_fmac_f32_e32 v161, v173, v169
	v_lshlrev_b32_e32 v168, 16, v132
	v_mul_f32_e32 v160, v160, v168
	v_and_b32_e32 v169, 0xffff0000, v132
	v_mul_f32_e32 v161, v161, v169
	v_lshlrev_b32_e32 v168, 16, v117
	v_fmac_f32_e32 v162, v173, v168
	v_and_b32_e32 v169, 0xffff0000, v117
	v_fmac_f32_e32 v163, v173, v169
	v_lshlrev_b32_e32 v168, 16, v133
	v_mul_f32_e32 v162, v162, v168
	v_and_b32_e32 v169, 0xffff0000, v133
	v_mul_f32_e32 v163, v163, v169
	v_lshlrev_b32_e32 v168, 16, v118
	v_fmac_f32_e32 v164, v173, v168
	v_and_b32_e32 v169, 0xffff0000, v118
	v_fmac_f32_e32 v165, v173, v169
	v_lshlrev_b32_e32 v168, 16, v134
	v_mul_f32_e32 v164, v164, v168
	v_and_b32_e32 v169, 0xffff0000, v134
	v_mul_f32_e32 v165, v165, v169
	v_lshlrev_b32_e32 v168, 16, v119
	v_fmac_f32_e32 v166, v173, v168
	v_and_b32_e32 v169, 0xffff0000, v119
	v_fmac_f32_e32 v167, v173, v169
	v_lshlrev_b32_e32 v168, 16, v135
	v_mul_f32_e32 v166, v166, v168
	v_and_b32_e32 v169, 0xffff0000, v135
	v_mul_f32_e32 v167, v167, v169
	v_cvt_pk_bf16_f32 v184, v160, v161
	v_cvt_pk_bf16_f32 v185, v162, v163
	v_cvt_pk_bf16_f32 v186, v164, v165
	v_cvt_pk_bf16_f32 v187, v166, v167
	global_store_dwordx4 v5, v[184:187], s[12:13] offset:1024
	v_lshlrev_b32_e32 v168, 16, v88
	v_lshlrev_b32_e32 v169, 16, v104
	v_add_f32_e32 v160, v168, v169
	v_and_b32_e32 v168, 0xffff0000, v88
	v_and_b32_e32 v169, 0xffff0000, v104
	v_add_f32_e32 v161, v168, v169
	v_lshlrev_b32_e32 v168, 16, v89
	v_lshlrev_b32_e32 v169, 16, v105
	v_add_f32_e32 v162, v168, v169
	v_and_b32_e32 v168, 0xffff0000, v89
	v_and_b32_e32 v169, 0xffff0000, v105
	v_add_f32_e32 v163, v168, v169
	v_lshlrev_b32_e32 v168, 16, v90
	v_lshlrev_b32_e32 v169, 16, v106
	v_add_f32_e32 v164, v168, v169
	v_and_b32_e32 v168, 0xffff0000, v90
	v_and_b32_e32 v169, 0xffff0000, v106
	v_add_f32_e32 v165, v168, v169
	v_lshlrev_b32_e32 v168, 16, v91
	v_lshlrev_b32_e32 v169, 16, v107
	v_add_f32_e32 v166, v168, v169
	v_and_b32_e32 v168, 0xffff0000, v91
	v_and_b32_e32 v169, 0xffff0000, v107
	v_add_f32_e32 v167, v168, v169
	v_add_f32_e32 v170, v160, v161
	v_add_f32_e32 v170, v170, v162
	v_add_f32_e32 v170, v170, v163
	v_add_f32_e32 v170, v170, v164
	v_add_f32_e32 v170, v170, v165
	v_add_f32_e32 v170, v170, v166
	v_add_f32_e32 v170, v170, v167
	s_nop 1
	v_add_f32_dpp v170, v170, v170 quad_perm:[1,0,3,2] row_mask:0xf bank_mask:0xf bound_ctrl:1
	s_nop 1
	v_add_f32_dpp v170, v170, v170 quad_perm:[2,3,0,1] row_mask:0xf bank_mask:0xf bound_ctrl:1
	s_nop 1
	v_add_f32_dpp v170, v170, v170 row_half_mirror row_mask:0xf bank_mask:0xf bound_ctrl:1
	v_mul_f32_e32 v170, 0x3c800000, v170
	v_sub_f32_e32 v160, v160, v170
	v_sub_f32_e32 v161, v161, v170
	v_sub_f32_e32 v162, v162, v170
	v_sub_f32_e32 v163, v163, v170
	v_sub_f32_e32 v164, v164, v170
	v_sub_f32_e32 v165, v165, v170
	v_sub_f32_e32 v166, v166, v170
	v_sub_f32_e32 v167, v167, v170
	v_mul_f32_e32 v171, v160, v160
	v_fmac_f32_e32 v171, v161, v161
	v_fmac_f32_e32 v171, v162, v162
	v_fmac_f32_e32 v171, v163, v163
	v_fmac_f32_e32 v171, v164, v164
	v_fmac_f32_e32 v171, v165, v165
	v_fmac_f32_e32 v171, v166, v166
	v_fmac_f32_e32 v171, v167, v167
	s_nop 1
	v_add_f32_dpp v171, v171, v171 quad_perm:[1,0,3,2] row_mask:0xf bank_mask:0xf bound_ctrl:1
	s_nop 1
	v_add_f32_dpp v171, v171, v171 quad_perm:[2,3,0,1] row_mask:0xf bank_mask:0xf bound_ctrl:1
	s_nop 1
	v_add_f32_dpp v171, v171, v171 row_half_mirror row_mask:0xf bank_mask:0xf bound_ctrl:1
	v_mov_b32_e32 v172, 0x3a27c5ac
	v_fmac_f32_e32 v172, 0x3c800000, v171
	v_rsq_f32_e32 v172, v172
	v_add_f32_e32 v173, v146, v150
	s_nop 0
	v_mul_f32_e32 v160, v160, v172
	v_mul_f32_e32 v161, v161, v172
	v_mul_f32_e32 v162, v162, v172
	v_mul_f32_e32 v163, v163, v172
	v_mul_f32_e32 v164, v164, v172
	v_mul_f32_e32 v165, v165, v172
	v_mul_f32_e32 v166, v166, v172
	v_mul_f32_e32 v167, v167, v172
	v_fma_f32 v160, v26, v160, v58
	v_fma_f32 v161, v27, v161, v59
	v_fma_f32 v162, v28, v162, v60
	v_fma_f32 v163, v29, v163, v61
	v_fma_f32 v164, v30, v164, v62
	v_fma_f32 v165, v31, v165, v63
	v_fma_f32 v166, v32, v166, v64
	v_fma_f32 v167, v33, v167, v65
	v_lshlrev_b32_e32 v168, 16, v120
	v_fmac_f32_e32 v160, v173, v168
	v_and_b32_e32 v169, 0xffff0000, v120
	v_fmac_f32_e32 v161, v173, v169
	v_lshlrev_b32_e32 v168, 16, v136
	v_mul_f32_e32 v160, v160, v168
	v_and_b32_e32 v169, 0xffff0000, v136
	v_mul_f32_e32 v161, v161, v169
	v_lshlrev_b32_e32 v168, 16, v121
	v_fmac_f32_e32 v162, v173, v168
	v_and_b32_e32 v169, 0xffff0000, v121
	v_fmac_f32_e32 v163, v173, v169
	v_lshlrev_b32_e32 v168, 16, v137
	v_mul_f32_e32 v162, v162, v168
	v_and_b32_e32 v169, 0xffff0000, v137
	v_mul_f32_e32 v163, v163, v169
	v_lshlrev_b32_e32 v168, 16, v122
	v_fmac_f32_e32 v164, v173, v168
	v_and_b32_e32 v169, 0xffff0000, v122
	v_fmac_f32_e32 v165, v173, v169
	v_lshlrev_b32_e32 v168, 16, v138
	v_mul_f32_e32 v164, v164, v168
	v_and_b32_e32 v169, 0xffff0000, v138
	v_mul_f32_e32 v165, v165, v169
	v_lshlrev_b32_e32 v168, 16, v123
	v_fmac_f32_e32 v166, v173, v168
	v_and_b32_e32 v169, 0xffff0000, v123
	v_fmac_f32_e32 v167, v173, v169
	v_lshlrev_b32_e32 v168, 16, v139
	v_mul_f32_e32 v166, v166, v168
	v_and_b32_e32 v169, 0xffff0000, v139
	v_mul_f32_e32 v167, v167, v169
	v_cvt_pk_bf16_f32 v192, v160, v161
	v_cvt_pk_bf16_f32 v193, v162, v163
	v_cvt_pk_bf16_f32 v194, v164, v165
	v_cvt_pk_bf16_f32 v195, v166, v167
	global_store_dwordx4 v5, v[192:195], s[12:13] offset:2048
	v_lshlrev_b32_e32 v168, 16, v92
	v_lshlrev_b32_e32 v169, 16, v108
	v_add_f32_e32 v160, v168, v169
	v_and_b32_e32 v168, 0xffff0000, v92
	v_and_b32_e32 v169, 0xffff0000, v108
	v_add_f32_e32 v161, v168, v169
	v_lshlrev_b32_e32 v168, 16, v93
	v_lshlrev_b32_e32 v169, 16, v109
	v_add_f32_e32 v162, v168, v169
	v_and_b32_e32 v168, 0xffff0000, v93
	v_and_b32_e32 v169, 0xffff0000, v109
	v_add_f32_e32 v163, v168, v169
	v_lshlrev_b32_e32 v168, 16, v94
	v_lshlrev_b32_e32 v169, 16, v110
	v_add_f32_e32 v164, v168, v169
	v_and_b32_e32 v168, 0xffff0000, v94
	v_and_b32_e32 v169, 0xffff0000, v110
	v_add_f32_e32 v165, v168, v169
	v_lshlrev_b32_e32 v168, 16, v95
	v_lshlrev_b32_e32 v169, 16, v111
	v_add_f32_e32 v166, v168, v169
	v_and_b32_e32 v168, 0xffff0000, v95
	v_and_b32_e32 v169, 0xffff0000, v111
	v_add_f32_e32 v167, v168, v169
	v_add_f32_e32 v170, v160, v161
	v_add_f32_e32 v170, v170, v162
	v_add_f32_e32 v170, v170, v163
	v_add_f32_e32 v170, v170, v164
	v_add_f32_e32 v170, v170, v165
	v_add_f32_e32 v170, v170, v166
	v_add_f32_e32 v170, v170, v167
	s_nop 1
	v_add_f32_dpp v170, v170, v170 quad_perm:[1,0,3,2] row_mask:0xf bank_mask:0xf bound_ctrl:1
	s_nop 1
	v_add_f32_dpp v170, v170, v170 quad_perm:[2,3,0,1] row_mask:0xf bank_mask:0xf bound_ctrl:1
	s_nop 1
	v_add_f32_dpp v170, v170, v170 row_half_mirror row_mask:0xf bank_mask:0xf bound_ctrl:1
	v_mul_f32_e32 v170, 0x3c800000, v170
	v_sub_f32_e32 v160, v160, v170
	v_sub_f32_e32 v161, v161, v170
	v_sub_f32_e32 v162, v162, v170
	v_sub_f32_e32 v163, v163, v170
	v_sub_f32_e32 v164, v164, v170
	v_sub_f32_e32 v165, v165, v170
	v_sub_f32_e32 v166, v166, v170
	v_sub_f32_e32 v167, v167, v170
	v_mul_f32_e32 v171, v160, v160
	v_fmac_f32_e32 v171, v161, v161
	v_fmac_f32_e32 v171, v162, v162
	v_fmac_f32_e32 v171, v163, v163
	v_fmac_f32_e32 v171, v164, v164
	v_fmac_f32_e32 v171, v165, v165
	v_fmac_f32_e32 v171, v166, v166
	v_fmac_f32_e32 v171, v167, v167
	s_nop 1
	v_add_f32_dpp v171, v171, v171 quad_perm:[1,0,3,2] row_mask:0xf bank_mask:0xf bound_ctrl:1
	s_nop 1
	v_add_f32_dpp v171, v171, v171 quad_perm:[2,3,0,1] row_mask:0xf bank_mask:0xf bound_ctrl:1
	s_nop 1
	v_add_f32_dpp v171, v171, v171 row_half_mirror row_mask:0xf bank_mask:0xf bound_ctrl:1
	v_mov_b32_e32 v172, 0x3a27c5ac
	v_fmac_f32_e32 v172, 0x3c800000, v171
	v_rsq_f32_e32 v172, v172
	v_add_f32_e32 v173, v147, v151
	s_nop 0
	v_mul_f32_e32 v160, v160, v172
	v_mul_f32_e32 v161, v161, v172
	v_mul_f32_e32 v162, v162, v172
	v_mul_f32_e32 v163, v163, v172
	v_mul_f32_e32 v164, v164, v172
	v_mul_f32_e32 v165, v165, v172
	v_mul_f32_e32 v166, v166, v172
	v_mul_f32_e32 v167, v167, v172
	v_fma_f32 v160, v34, v160, v66
	v_fma_f32 v161, v35, v161, v67
	v_fma_f32 v162, v36, v162, v68
	v_fma_f32 v163, v37, v163, v69
	v_fma_f32 v164, v38, v164, v70
	v_fma_f32 v165, v39, v165, v71
	v_fma_f32 v166, v40, v166, v72
	v_fma_f32 v167, v41, v167, v73
	v_lshlrev_b32_e32 v168, 16, v124
	v_fmac_f32_e32 v160, v173, v168
	v_and_b32_e32 v169, 0xffff0000, v124
	v_fmac_f32_e32 v161, v173, v169
	v_lshlrev_b32_e32 v168, 16, v140
	v_mul_f32_e32 v160, v160, v168
	v_and_b32_e32 v169, 0xffff0000, v140
	v_mul_f32_e32 v161, v161, v169
	v_lshlrev_b32_e32 v168, 16, v125
	v_fmac_f32_e32 v162, v173, v168
	v_and_b32_e32 v169, 0xffff0000, v125
	v_fmac_f32_e32 v163, v173, v169
	v_lshlrev_b32_e32 v168, 16, v141
	v_mul_f32_e32 v162, v162, v168
	v_and_b32_e32 v169, 0xffff0000, v141
	v_mul_f32_e32 v163, v163, v169
	v_lshlrev_b32_e32 v168, 16, v126
	v_fmac_f32_e32 v164, v173, v168
	v_and_b32_e32 v169, 0xffff0000, v126
	v_fmac_f32_e32 v165, v173, v169
	v_lshlrev_b32_e32 v168, 16, v142
	v_mul_f32_e32 v164, v164, v168
	v_and_b32_e32 v169, 0xffff0000, v142
	v_mul_f32_e32 v165, v165, v169
	v_lshlrev_b32_e32 v168, 16, v127
	v_fmac_f32_e32 v166, v173, v168
	v_and_b32_e32 v169, 0xffff0000, v127
	v_fmac_f32_e32 v167, v173, v169
	v_lshlrev_b32_e32 v168, 16, v143
	v_mul_f32_e32 v166, v166, v168
	v_and_b32_e32 v169, 0xffff0000, v143
	v_mul_f32_e32 v167, v167, v169
	v_cvt_pk_bf16_f32 v196, v160, v161
	v_cvt_pk_bf16_f32 v197, v162, v163
	v_cvt_pk_bf16_f32 v198, v164, v165
	v_cvt_pk_bf16_f32 v199, v166, v167
	global_store_dwordx4 v5, v[196:199], s[12:13] offset:3072
	s_add_i32 s24, s24, 1
	s_cmp_lt_u32 s24, 32
	s_cbranch_scc1 .Lx14_row

.LBB0_1866:
	s_cmp_lt_i32 s72, 15
	s_cselect_b64 s[4:5], -1, 0
	s_and_b64 s[0:1], s[4:5], s[6:7]
	s_andn2_b64 vcc, exec, s[0:1]
	s_cmp_eq_u32 s33, 0x100
	s_cbranch_scc1 .LBB0_1872
	s_cbranch_vccnz .LBB0_1872
	s_lshl_b32 s0, s2, 3
	s_add_i32 s6, s82, s0
	s_cmpk_gt_i32 s6, 0x7fff
	s_cbranch_scc1 .LBB0_1872
	s_add_u32 s0, s54, 0x8c00000
	s_addc_u32 s1, s55, 0
	s_add_u32 s8, s54, 0x29400000
	s_addc_u32 s9, s55, 0
	s_add_u32 s10, s54, 0x21200000
	s_addc_u32 s11, s55, 0
	s_add_u32 s12, s54, 0x49c00000
	s_addc_u32 s13, s55, 0
	v_and_b32_e32 v1, 63, v0
	s_ashr_i32 s7, s6, 31
	s_lshl_b64 s[14:15], s[6:7], 12
	v_lshlrev_b32_e32 v22, 4, v1
	v_or_b32_e32 v146, s14, v22
	v_mov_b32_e32 v147, s15
	v_lshl_add_u64 v[2:3], s[0:1], 0, v[146:147]
	v_lshl_add_u64 v[4:5], s[8:9], 0, v[146:147]
	global_load_dwordx4 v[126:129], v[2:3], off
	global_load_dwordx4 v[122:125], v[4:5], off
	v_lshl_add_u64 v[2:3], s[10:11], 0, v[146:147]
	v_lshl_add_u64 v[4:5], s[12:13], 0, v[146:147]
	global_load_dwordx4 v[118:121], v[2:3], off
	global_load_dwordx4 v[106:109], v[4:5], off
	v_or_b32_e32 v2, 0x400, v146
	v_mov_b32_e32 v3, s15
	v_lshl_add_u64 v[4:5], s[0:1], 0, v[2:3]
	v_lshl_add_u64 v[6:7], s[8:9], 0, v[2:3]
	global_load_dwordx4 v[114:117], v[4:5], off
	global_load_dwordx4 v[110:113], v[6:7], off
	v_lshl_add_u64 v[4:5], s[10:11], 0, v[2:3]
	v_lshl_add_u64 v[2:3], s[12:13], 0, v[2:3]
	global_load_dwordx4 v[102:105], v[4:5], off
	global_load_dwordx4 v[98:101], v[2:3], off
	v_or_b32_e32 v2, 0x800, v146
	v_mov_b32_e32 v3, s15
	v_lshl_add_u64 v[4:5], s[0:1], 0, v[2:3]
	v_lshl_add_u64 v[6:7], s[8:9], 0, v[2:3]
	global_load_dwordx4 v[94:97], v[4:5], off
	global_load_dwordx4 v[90:93], v[6:7], off
	v_lshl_add_u64 v[4:5], s[10:11], 0, v[2:3]
	v_lshl_add_u64 v[2:3], s[12:13], 0, v[2:3]
	global_load_dwordx4 v[14:17], v[4:5], off
	global_load_dwordx4 v[10:13], v[2:3], off
	v_or_b32_e32 v2, 0xc00, v146
	v_mov_b32_e32 v3, s15
	v_lshl_add_u64 v[4:5], s[0:1], 0, v[2:3]
	v_lshl_add_u64 v[6:7], s[8:9], 0, v[2:3]
	v_lshl_add_u64 v[18:19], s[10:11], 0, v[2:3]
	global_load_dwordx4 v[86:89], v[4:5], off
	global_load_dwordx4 v[82:85], v[6:7], off
	v_lshl_add_u64 v[20:21], s[12:13], 0, v[2:3]
	global_load_dwordx4 v[6:9], v[18:19], off
	global_load_dwordx4 v[2:5], v[20:21], off
	s_load_dwordx4 s[12:15], s[74:75], 0x100
	s_lshl_b32 s8, s33, 3
	v_lshlrev_b32_e32 v18, 5, v1
	s_lshl_b64 s[0:1], s[6:7], 7
	v_lshrrev_b32_e32 v1, 1, v0
	v_and_or_b32 v160, v1, 28, s0
	s_add_i32 s0, s6, s8
	v_mov_b32_e32 v19, 0
	v_mov_b32_e32 v161, s1
	s_ashr_i32 s1, s0, 31
	s_waitcnt lgkmcnt(0)
	v_lshl_add_u64 v[148:149], s[12:13], 0, v[18:19]
	v_lshl_add_u64 v[150:151], s[14:15], 0, v[18:19]
	v_or_b32_e32 v20, 0x1000, v18
	v_mov_b32_e32 v21, v19
	v_or_b32_e32 v18, 0x1800, v18
	s_ashr_i32 s9, s8, 31
	s_lshl_b64 s[0:1], s[0:1], 12
	v_lshl_add_u64 v[152:153], s[12:13], 0, v[20:21]
	v_lshl_add_u64 v[154:155], s[14:15], 0, v[20:21]
	v_lshl_add_u64 v[156:157], s[12:13], 0, v[18:19]
	v_lshl_add_u64 v[158:159], s[14:15], 0, v[18:19]
	s_lshl_b64 s[10:11], s[8:9], 12
	s_lshl_b64 s[12:13], s[8:9], 7
	v_or_b32_e32 v162, s0, v22
	v_mov_b32_e32 v163, s1
	s_mov_b32 s3, 0xc00000
	s_mov_b32 s7, 0x1000000
	s_mov_b32 s14, 0x3c800000
	s_mov_b32 s16, 0x3a27c5ac
	s_mov_b32 s9, 0x800000
	s_mov_b32 s15, 0x19000000
	s_branch .LBB0_1870

.LBB0_1872:
	s_cmp_gt_i32 s73, 15
	s_cselect_b64 s[6:7], -1, 0
	s_and_b64 s[0:1], s[4:5], s[6:7]
	s_andn2_b64 vcc, exec, s[0:1]
	s_cmp_eq_u32 s33, 0x100
	s_cbranch_scc1 .LBB0_1922
	s_cbranch_vccnz .LBB0_1922
	s_waitcnt vmcnt(0)
	v_cmp_eq_u32_e32 vcc, 0, v0
	s_waitcnt vmcnt(0)
	s_barrier
	s_and_saveexec_b64 s[4:5], vcc
	s_cbranch_execz .LBB0_1921
	s_add_i32 s0, 0, 0x27800
	v_mov_b32_e32 v1, s0
	s_waitcnt vmcnt(0) expcnt(0) lgkmcnt(0)
	ds_read_b32 v3, v1
	s_add_i32 s0, 0, 0x27804
	v_mov_b32_e32 v1, s0
	ds_read_b32 v1, v1
	s_waitcnt lgkmcnt(1)
	v_cmp_ne_u32_e32 vcc, 0, v3
	s_cbranch_vccnz .LBB0_1889
	v_readlane_b32 s8, v255, 0
	v_readlane_b32 s9, v255, 1
	s_load_dwordx2 s[0:1], s[8:9], 0x4
	s_add_u32 s8, s54, 0x1000
	s_addc_u32 s9, s55, 0
	s_add_u32 s10, s54, 0x1100
	s_addc_u32 s11, s55, 0
	s_add_u32 s12, s54, 0x1200
	s_addc_u32 s13, s55, 0
	s_waitcnt lgkmcnt(0)
	s_mul_i32 s3, s0, s33
	s_add_u32 s14, s54, 0x1300
	s_mul_i32 s3, s3, s1
	s_addc_u32 s15, s55, 0
	s_mov_b32 s22, 1
	v_mov_b32_e32 v17, 0
	s_branch .LBB0_1877
